# second redundant barrier removed: the first barrier of the attention queue pop (the unit's key-tile barriers already separate the previous slot reads from the next slot write)
# baseline (speedup 1.0000x reference)
.LBB0_262:
	s_and_saveexec_b64 s[10:11], s[38:39]
	s_cbranch_execz .LBB0_266
	s_mov_b64 s[42:43], exec
	v_mbcnt_lo_u32_b32 v0, s42, 0
	v_mbcnt_hi_u32_b32 v0, s43, v0
	v_cmp_eq_u32_e32 vcc, 0, v0
	s_and_saveexec_b64 s[40:41], vcc
	s_cbranch_execz .LBB0_265
	s_bcnt1_i32_b64 s12, s[42:43]
	v_readlane_b32 s4, v255, 15
	v_mov_b32_e32 v2, s12
	v_readlane_b32 s5, v255, 16
	s_nop 4
	global_atomic_add v2, v1, v2, s[4:5] sc0
